# idle WGs of the in-projection 4th round (bid>=48) convert 6 background steps there (branch into bg_take and back); attention quotas 20/20 + balance deltas
# speedup vs baseline: 1.0124x; 1.0009x over previous
; #define LAS __attribute__((address_space(3)))
; __global__ void __launch_bounds__(512, 2) mk_fwd(Args a) {
;     extern __shared__ __attribute__((aligned(16))) unsigned char lds_raw[];
;     Ctx c; c.lds = (LAS unsigned char*)lds_raw; c.tid = threadIdx.x; c.lane = c.tid & 63; c.wave = __builtin_amdgcn_readfirstlane(c.tid >> 6); c.bid = blockIdx.x; c.G = gridDim.x;
;     volatile LAS unsigned* MISC = (volatile LAS unsigned*)(c.lds + LDS_MISC);
;     if (c.tid < 32) MISC[c.tid] = 0u;
;     __syncthreads();
;     XcdBarrier bar; bar.bar = (unsigned*)(a.ws + WS_CTL) + 4096; bar.x = 0; bar.st = nullptr;
;     const int lo = a.ph_lo, hi = a.ph_hi;
;     if (hi - lo > 1) bar = xcd_barrier_post((unsigned*)(a.ws + WS_CTL) + 4096, MISC + 8);
_Z6mk_fwd4Args:
	v_writelane_b32 v255, 0, 42
	s_mov_b64 s[36:37], s[0:1]
	s_load_dword s91, s[0:1], 0xf0
	s_add_u32 s0, s36, 0xf0
	s_addc_u32 s1, s37, 0
	s_mov_b32 s90, s2
	v_writelane_b32 v252, s0, 0
	v_cmp_gt_u32_e32 vcc, 32, v0
	s_nop 0
	v_writelane_b32 v252, s1, 1
	s_and_saveexec_b64 s[0:1], vcc
	v_lshl_add_u32 v1, v0, 2, 0
	v_add_u32_e32 v1, 0x27000, v1
	v_mov_b32_e32 v2, 0
	ds_write_b32 v1, v2
	s_or_b64 exec, exec, s[0:1]
	s_load_dwordx4 s[68:71], s[36:37], 0xe0
	s_mov_b32 s33, 0
	v_cmp_eq_u32_e32 vcc, 0, v0
	s_waitcnt lgkmcnt(0)
	s_barrier
	s_add_u32 s0, s68, 0x4000
	s_addc_u32 s1, s69, 0
	s_sub_i32 s2, s71, s70
	v_writelane_b32 v252, s0, 2
	s_cmp_gt_i32 s2, 1
	s_nop 0
	v_writelane_b32 v252, s1, 3
	s_cselect_b64 s[0:1], -1, 0
	s_cmp_lt_i32 s2, 2
	s_mov_b32 s2, 0
	v_writelane_b32 v252, s2, 4
	s_cbranch_scc1 .LBB0_8
	s_getreg_b32 s2, hwreg(HW_REG_XCC_ID, 0, 4)
	s_and_b32 s33, s2, 15
	s_and_saveexec_b64 s[2:3], vcc
	s_cbranch_execz .LBB0_7
	s_mov_b64 s[6:7], exec
	v_mbcnt_lo_u32_b32 v1, s6, 0
	v_mbcnt_hi_u32_b32 v1, s7, v1
	v_cmp_eq_u32_e32 vcc, 0, v1
	s_and_saveexec_b64 s[4:5], vcc
	s_cbranch_execz .LBB0_6
	s_bcnt1_i32_b64 s6, s[6:7]
	s_lshl_b32 s8, s33, 8
	v_mov_b32_e32 v3, s6
	v_readlane_b32 s6, v252, 2
	v_mov_b32_e32 v2, s8
	v_readlane_b32 s7, v252, 3
	s_nop 4
	global_atomic_add v2, v2, v3, s[6:7] offset:1024 sc0

; #define LAS __attribute__((address_space(3)))
; #define PHASE_BEGIN() Ctx c = c0; { int t_ = c0.tid; asm volatile("" : "+v"(t_)); c.tid = t_; c.lane = t_ & 63; c.wave = __builtin_amdgcn_readfirstlane(t_ >> 6); } \
;     GAS unsigned char* wsb = (GAS unsigned char*)a.ws; asm volatile("" : "+s"(wsb));
; #define SEAM(k) do { if (IN(k) && IN((k) + 1)) { XcdBarrier b_ = bar; { GAS unsigned* t_ = (GAS unsigned*)b_.bar; asm volatile("" : "+s"(t_)); b_.bar = (unsigned*)t_; } xcd_barrier(b_); } } while (0)
; __device__ __forceinline__ void bg_take(const Args& a, const Ctx& c0, int n) {
;     PHASE_BEGIN();
;     unsigned* head = WSP(unsigned, WS_CTL) + CW_QHEAD;
;     volatile LAS unsigned* bc = (volatile LAS unsigned*)(c.lds + LDS_MISC + 64);
;     LAS float* scr = (LAS float*)(c.lds + c.wave * 16640);
;     __syncthreads();
;     for (int i = 0; i < n; ++i) {
;         if (c.tid == 0) { unsigned s = __hip_atomic_fetch_add(head, 1u, __ATOMIC_RELAXED, __HIP_MEMORY_SCOPE_AGENT); if (s >= (unsigned)BG_STEPS) s = 0xffffffffu; bc[0] = s; }
; __global__ void __launch_bounds__(512, 2) mk_fwd(Args a) {
;     ...
;             pg8::gemm_phase(c.lds, p); }
;     ...
;         if (IN(pb + 1)) bg_fill(a, c, l * 8 + 1, 0);
;     ...
;         SEAM(pb + 1);
.LBB0_322:
	v_readlane_b32 s2, v255, 42
	s_nop 3
	s_cmp_lg_u32 s2, 0
	s_cbranch_scc1 .Ltail_ret
	s_cmp_lt_u32 s90, 48
	s_cbranch_scc1 .Ltail_cont
	v_writelane_b32 v255, 1, 42
	s_mov_b32 s30, 0xc3e00000
	s_movk_i32 s78, 0x315c
	v_readlane_b32 s76, v254, 53
	s_mov_b32 s81, 0x10000
	s_mov_b32 s82, 0x18000
	s_mov_b32 s83, 0x8000
	s_mov_b32 s86, 0xc000
	s_mov_b32 s14, 6
	s_branch .Lbt1_entry
.Ltail_ret:
	v_writelane_b32 v255, 0, 42
	s_mov_b64 s[20:21], 0x2000

; __global__ void __launch_bounds__(512, 2) mk_fwd(Args a) {
;     ...
;         if (IN(pb + 5) && (c.bid & 1) == 0) { if (l == 0) mod_items(a, c, 1); bg_take(a, c, l == 0 ? 26 : 24); }
;         if (EN(5) && IN(pb + 5)) for (int rep = 0; rep < NREP(5); ++rep) { phase_attn(a, c, l, last); }
;         if (IN(pb + 5) && (c.bid & 1) == 1) { bg_take(a, c, l == 0 ? 26 : 24); if (l == 0) mod_items(a, c, 1); }
.LBB0_1254:
	s_cmp_lt_u32 s14, 25
	s_cbranch_scc1 .Lbal1_l1
	s_mov_b32 s14, 20
	s_cmp_lt_u32 s90, 32
	s_cbranch_scc0 .Lbal1_b
	s_add_i32 s14, s14, -4
.Lbal1_b:
	s_cmp_gt_u32 s90, 191
	s_cbranch_scc0 .Lbal1_c
	s_add_i32 s14, s14, 3
	s_branch .Lbal1_c
.Lbal1_l1:
	s_mov_b32 s14, 20

; #define LAS __attribute__((address_space(3)))
; #define PHASE_BEGIN() Ctx c = c0; { int t_ = c0.tid; asm volatile("" : "+v"(t_)); c.tid = t_; c.lane = t_ & 63; c.wave = __builtin_amdgcn_readfirstlane(t_ >> 6); } \
;     GAS unsigned char* wsb = (GAS unsigned char*)a.ws; asm volatile("" : "+s"(wsb));
; __device__ __forceinline__ void bg_take(const Args& a, const Ctx& c0, int n) {
;     PHASE_BEGIN();
;     unsigned* head = WSP(unsigned, WS_CTL) + CW_QHEAD;
;     volatile LAS unsigned* bc = (volatile LAS unsigned*)(c.lds + LDS_MISC + 64);
;     LAS float* scr = (LAS float*)(c.lds + c.wave * 16640);
;     __syncthreads();
.Lbal1_d:
.Lbt1_entry:
	v_mov_b32_e32 v2, v0
	v_readlane_b32 s8, v254, 21
	v_readlane_b32 s10, v254, 23
	v_readfirstlane_b32 s2, v2
	v_readlane_b32 s11, v254, 24
	s_ashr_i32 s15, s2, 6
	s_mov_b64 s[6:7], s[10:11]
	s_waitcnt lgkmcnt(0)
	v_lshlrev_b32_e32 v3, 2, v2
	s_add_u32 s2, s6, 0x8000
	s_mul_i32 s8, s15, 0x4100
	v_bfe_u32 v67, v2, 4, 2
	v_and_b32_e32 v66, 60, v3
	s_addc_u32 s3, s7, 0
	s_add_i32 s8, s8, 0
	v_cmp_eq_u32_e64 s[40:41], 0, v2
	v_mul_u32_u24_e32 v3, 0x104, v67
	v_lshlrev_b32_e32 v4, 2, v66
	v_bfe_u32 v96, v2, 3, 3
	v_lshlrev_b32_e32 v2, 3, v2
	v_add3_u32 v95, s8, v3, v4
	v_and_b32_e32 v2, 56, v2
	v_mov_b32_e32 v3, v147
	v_mul_u32_u24_e32 v6, 0x104, v2
	v_lshl_add_u64 v[4:5], s[6:7], 0, v[2:3]
	v_lshlrev_b32_e32 v3, 2, v96
	v_add3_u32 v97, s8, v6, v3
	v_lshlrev_b32_e32 v2, 1, v2
	v_mov_b32_e32 v3, v147
	v_lshl_add_u64 v[2:3], s[6:7], 0, v[2:3]
	s_mov_b64 s[6:7], 0x1bc00000
	v_lshl_add_u64 v[72:73], v[2:3], 0, s[6:7]
	s_mov_b64 s[6:7], 0x1b800000
	v_lshl_add_u64 v[74:75], v[2:3], 0, s[6:7]
	s_mov_b64 s[6:7], 0x1b600000
	v_lshl_add_u64 v[76:77], v[2:3], 0, s[6:7]
	s_mov_b64 s[6:7], 0x1aa00000
	v_lshl_add_u64 v[78:79], v[2:3], 0, s[6:7]
	s_mov_b64 s[6:7], 0x12a00000
	v_lshl_add_u64 v[80:81], v[4:5], 0, s[6:7]
	s_mov_b64 s[6:7], 0x2a00000
	v_lshl_add_u64 v[82:83], v[4:5], 0, s[6:7]
	s_mov_b64 s[6:7], 0x2200000
	v_lshl_add_u64 v[84:85], v[2:3], 0, s[6:7]
	s_mov_b64 s[6:7], 0x1e00000
	v_readlane_b32 s9, v254, 22
	v_lshl_add_u64 v[86:87], v[2:3], 0, s[6:7]
	s_mov_b64 s[6:7], 0x1c00000
	s_mov_b64 s[10:11], 0x2c400000
	s_mov_b64 s[8:9], 0x1c400000
	v_lshl_add_u64 v[88:89], v[2:3], 0, s[6:7]
	s_mov_b64 s[6:7], 0x1000000
	v_lshl_add_u64 v[68:69], v[4:5], 0, s[10:11]
	v_or_b32_e32 v98, 8, v96
	v_or_b32_e32 v99, 16, v96
	v_or_b32_e32 v100, 24, v96
	v_or_b32_e32 v101, 32, v96
	v_or_b32_e32 v102, 40, v96
	v_or_b32_e32 v103, 48, v96
	v_or_b32_e32 v104, 56, v96
	v_lshl_add_u64 v[70:71], v[4:5], 0, s[8:9]
	v_lshl_add_u64 v[90:91], v[2:3], 0, s[6:7]
	s_waitcnt vmcnt(0)
	s_barrier
	s_branch .LBB0_1256

; #define SEAM(k) do { if (IN(k) && IN((k) + 1)) { XcdBarrier b_ = bar; { GAS unsigned* t_ = (GAS unsigned*)b_.bar; asm volatile("" : "+s"(t_)); b_.bar = (unsigned*)t_; } xcd_barrier(b_); } } while (0)
; __device__ __forceinline__ void bg_take(const Args& a, const Ctx& c0, int n) {
;     ...
;         __syncthreads();
;     }
;     __syncthreads();
; __global__ void __launch_bounds__(512, 2) mk_fwd(Args a) {
;     ...
;             pg8::gemm_phase(c.lds, p); }
;     ...
;         if (IN(pb + 1)) bg_fill(a, c, l * 8 + 1, 0);
;     ...
;         SEAM(pb + 1);
.LBB0_1441:
	s_barrier
	v_readlane_b32 s2, v255, 42
	s_nop 3
	s_cmp_eq_u32 s2, 1
	s_cbranch_scc0 .Lbt1_normal_exit
	v_writelane_b32 v255, 2, 42
	s_branch .LBB0_321
.Lbt1_normal_exit:
.LBB0_1442:
	s_xor_b64 s[2:3], s[4:5], -1
	s_andn2_b64 vcc, exec, s[2:3]
	s_mov_b64 s[2:3], -1
	s_cbranch_vccnz .LBB0_1444
	v_readlane_b32 s2, v254, 58
	s_add_i32 s12, s2, 7
	s_cbranch_execnz .LBB0_1751
	s_branch .LBB0_1445

; __global__ void __launch_bounds__(512, 2) mk_fwd(Args a) {
;     ...
;         if (IN(pb + 5) && (c.bid & 1) == 0) { if (l == 0) mod_items(a, c, 1); bg_take(a, c, l == 0 ? 26 : 24); }
;         if (EN(5) && IN(pb + 5)) for (int rep = 0; rep < NREP(5); ++rep) { phase_attn(a, c, l, last); }
;         if (IN(pb + 5) && (c.bid & 1) == 1) { bg_take(a, c, l == 0 ? 26 : 24); if (l == 0) mod_items(a, c, 1); }
.LBB0_1493:
	v_readlane_b32 s2, v252, 54
	v_readlane_b32 s3, v252, 55
	s_andn2_b64 vcc, exec, s[2:3]
	s_cbranch_vccnz .LBB0_1700
	v_readlane_b32 s2, v254, 54
	v_readlane_b32 s3, v254, 55
	s_and_b64 s[2:3], s[2:3], exec
	v_mov_b32_e32 v1, v0
	v_readlane_b32 s4, v254, 21
	v_readlane_b32 s5, v254, 22
	v_readfirstlane_b32 s2, v1
	v_readlane_b32 s6, v254, 23
	v_readlane_b32 s7, v254, 24
	s_cselect_b32 s10, 26, 24
	s_cmp_lt_u32 s10, 25
	s_cbranch_scc1 .Lbal2_l1
	s_mov_b32 s10, 20
	s_cmp_lt_u32 s90, 32
	s_cbranch_scc0 .Lbal2_b
	s_add_i32 s10, s10, -4
.Lbal2_b:
	s_cmp_gt_u32 s90, 191
	s_cbranch_scc0 .Lbal2_c
	s_add_i32 s10, s10, 3
	s_branch .Lbal2_c
.Lbal2_l1:
	s_mov_b32 s10, 20
.Lbal2_c:
	s_cmp_lt_u32 s90, 16
	s_cbranch_scc0 .Lbal2_d
	s_add_i32 s10, s10, -5
